# v18 + PEER phase build stage: the H2 int8 rows and selection-index loads (read once, then LDS-resident) marked nt so they do not displace the table slices in L2
# speedup vs baseline: 1.0103x; 1.0025x over previous
; #define GAS __attribute__((address_space(1)))
; #define LAS __attribute__((address_space(3)))
; DI void p9v2_phase(Frame& F) {
;     ...
;     for (int tb = (int)blockIdx.x * 64; tb < M; tb += F.G * 64) {
; #pragma unroll
;         for (int j = 0; j < 8; ++j) { const int tl = F.wave * 8 + j;
; #pragma unroll
;             for (int jj = 0; jj < 2; ++jj) *(LAS v4u*)(HQ + tl * 2048 + 1024 * jj + 16 * lane) = *(const GAS v4u*)(F.H2Q + (size_t)(tb + tl) * D + 1024 * jj + 16 * lane); }
;         if (tid < 64) SH[tid] = F.SA[tb + tid];
;         __syncthreads();
; #pragma unroll
;         for (int i = 0; i < 16; ++i) { const int q = tid + 512 * i, k = q & 127; IDX16[(q & ~127) + (k & 64) + 8 * (k & 7) + ((k >> 3) & 7)] = (unsigned short)F.IDX[(size_t)tb * NSEL + q]; }
;         __syncthreads();
.LBB0_1299:
	s_add_i32 s42, s22, s29
	s_ashr_i32 s43, s42, 31
	s_lshl_b64 s[14:15], s[42:43], 11
	v_lshl_add_u64 v[6:7], v[154:155], 0, s[14:15]
	s_add_i32 s14, s22, s35
	s_ashr_i32 s15, s14, 31
	s_lshl_b64 s[44:45], s[14:15], 11
	v_lshl_add_u64 v[14:15], v[154:155], 0, s[44:45]
	s_add_i32 s44, s22, s48
	s_ashr_i32 s45, s44, 31
	s_lshl_b64 s[44:45], s[44:45], 11
	v_lshl_add_u64 v[22:23], v[154:155], 0, s[44:45]
	s_add_i32 s44, s22, s50
	s_ashr_i32 s45, s44, 31
	s_lshl_b64 s[44:45], s[44:45], 11
	v_lshl_add_u64 v[30:31], v[154:155], 0, s[44:45]
	s_add_i32 s44, s22, s52
	s_ashr_i32 s45, s44, 31
	s_lshl_b64 s[44:45], s[44:45], 11
	s_waitcnt vmcnt(26)
	v_lshl_add_u64 v[38:39], v[154:155], 0, s[44:45]
	s_add_i32 s44, s22, s54
	s_ashr_i32 s45, s44, 31
	s_lshl_b64 s[44:45], s[44:45], 11
	s_waitcnt vmcnt(22)
	v_lshl_add_u64 v[46:47], v[154:155], 0, s[44:45]
	s_add_i32 s44, s22, s56
	s_ashr_i32 s45, s44, 31
	s_lshl_b64 s[44:45], s[44:45], 11
	s_waitcnt vmcnt(15)
	v_lshl_add_u64 v[54:55], v[154:155], 0, s[44:45]
	s_add_i32 s44, s22, s58
	s_ashr_i32 s45, s44, 31
	s_lshl_b64 s[44:45], s[44:45], 11
	s_waitcnt vmcnt(8)
	v_lshl_add_u64 v[62:63], v[154:155], 0, s[44:45]
	global_load_dwordx4 v[2:5], v[6:7], off nt
	s_nop 0
	global_load_dwordx4 v[6:9], v[6:7], off offset:1024 nt
	s_nop 0
	global_load_dwordx4 v[10:13], v[14:15], off nt
	s_nop 0
	global_load_dwordx4 v[14:17], v[14:15], off offset:1024 nt
	s_nop 0
	global_load_dwordx4 v[18:21], v[22:23], off nt
	s_nop 0
	global_load_dwordx4 v[22:25], v[22:23], off offset:1024 nt
	s_nop 0
	global_load_dwordx4 v[26:29], v[30:31], off nt
	s_nop 0
	global_load_dwordx4 v[30:33], v[30:31], off offset:1024 nt
	s_nop 0
	global_load_dwordx4 v[34:37], v[38:39], off nt
	s_nop 0
	global_load_dwordx4 v[38:41], v[38:39], off offset:1024 nt
	s_nop 0
	global_load_dwordx4 v[42:45], v[46:47], off nt
	s_nop 0
	global_load_dwordx4 v[46:49], v[46:47], off offset:1024 nt
	s_nop 0
	global_load_dwordx4 v[50:53], v[54:55], off nt
	s_nop 0
	global_load_dwordx4 v[54:57], v[54:55], off offset:1024 nt
	s_nop 0
	global_load_dwordx4 v[58:61], v[62:63], off nt
	s_nop 0
	global_load_dwordx4 v[62:65], v[62:63], off offset:1024 nt
	s_waitcnt vmcnt(21)
	v_add_u32_e32 v66, s31, v131
	s_waitcnt vmcnt(20)
	v_add_u32_e32 v67, s41, v131
	s_waitcnt vmcnt(19)
	v_add_u32_e32 v68, s49, v131
	s_waitcnt vmcnt(18)
	v_add_u32_e32 v69, s51, v131
	s_waitcnt vmcnt(17)
	v_add_u32_e32 v70, s53, v131
	s_waitcnt vmcnt(16)
	v_add_u32_e32 v71, s55, v131
	v_add_u32_e32 v72, s57, v131
	v_add_u32_e32 v73, s59, v131
	s_waitcnt vmcnt(15)
	ds_write_b128 v66, v[2:5]
	s_waitcnt vmcnt(14)
	ds_write_b128 v66, v[6:9] offset:1024
	s_waitcnt vmcnt(13)
	ds_write_b128 v67, v[10:13]
	s_waitcnt vmcnt(12)
	ds_write_b128 v67, v[14:17] offset:1024
	s_waitcnt vmcnt(11)
	ds_write_b128 v68, v[18:21]
	s_waitcnt vmcnt(10)
	ds_write_b128 v68, v[22:25] offset:1024
	s_waitcnt vmcnt(9)
	ds_write_b128 v69, v[26:29]
	s_waitcnt vmcnt(8)
	ds_write_b128 v69, v[30:33] offset:1024
	s_waitcnt vmcnt(7)
	ds_write_b128 v70, v[34:37]
	s_waitcnt vmcnt(6)
	ds_write_b128 v70, v[38:41] offset:1024
	s_waitcnt vmcnt(5)
	ds_write_b128 v71, v[42:45]
	s_waitcnt vmcnt(4)
	ds_write_b128 v71, v[46:49] offset:1024
	s_waitcnt vmcnt(3)
	ds_write_b128 v72, v[50:53]
	s_waitcnt vmcnt(2)
	ds_write_b128 v72, v[54:57] offset:1024
	s_waitcnt vmcnt(1)
	ds_write_b128 v73, v[58:61]
	s_waitcnt vmcnt(0)
	ds_write_b128 v73, v[62:65] offset:1024
	s_and_saveexec_b64 s[44:45], s[0:1]
	s_cbranch_execz .LBB0_1301
	v_or_b32_e32 v2, s22, v0
	v_ashrrev_i32_e32 v3, 31, v2
	v_lshl_add_u64 v[2:3], v[2:3], 2, s[64:65]
	global_load_dword v2, v[2:3], off
	s_waitcnt vmcnt(0)
	ds_write_b32 v158, v2
.LBB0_1301:
	s_or_b64 exec, exec, s[44:45]
	s_ashr_i32 s23, s22, 31
	s_lshl_b64 s[44:45], s[22:23], 9
	s_add_u32 s44, s16, s44
	s_addc_u32 s45, s17, s45
	v_lshl_add_u64 v[2:3], s[44:45], 0, v[146:147]
	v_add_co_u32_e32 v4, vcc, s27, v2
	s_waitcnt lgkmcnt(0)
	s_nop 0
	v_addc_co_u32_e32 v5, vcc, 0, v3, vcc
	v_add_co_u32_e32 v6, vcc, s68, v2
	s_barrier
	s_nop 0
	v_addc_co_u32_e32 v7, vcc, 0, v3, vcc
	v_add_co_u32_e32 v8, vcc, s69, v2
	s_nop 1
	v_addc_co_u32_e32 v9, vcc, 0, v3, vcc
	v_add_co_u32_e32 v10, vcc, s70, v2
	global_load_dword v19, v146, s[44:45] nt
	global_load_dword v20, v146, s[44:45] offset:2048 nt
	v_addc_co_u32_e32 v11, vcc, 0, v3, vcc
	global_load_dword v21, v188, s[44:45] nt
	global_load_dword v22, v[4:5], off offset:2048 nt
	global_load_dword v23, v189, s[44:45] nt
	global_load_dword v24, v[6:7], off offset:2048 nt
	global_load_dword v25, v190, s[44:45] nt
	global_load_dword v26, v[8:9], off offset:2048 nt
	global_load_dword v27, v191, s[44:45] nt
	global_load_dword v28, v[10:11], off offset:2048 nt
	v_add_co_u32_e32 v4, vcc, s71, v2
	s_mov_b32 s23, 0
	s_nop 0
	v_addc_co_u32_e32 v5, vcc, 0, v3, vcc
	v_add_co_u32_e32 v6, vcc, s72, v2
	v_mov_b32_e32 v8, 0
	s_nop 0
	v_addc_co_u32_e32 v7, vcc, 0, v3, vcc
	v_add_co_u32_e32 v2, vcc, 0x7000, v2
	v_mov_b32_e32 v9, 0
	s_nop 0
	v_addc_co_u32_e32 v3, vcc, 0, v3, vcc
	global_load_dword v29, v192, s[44:45] nt
	s_nop 0
	global_load_dword v4, v[4:5], off offset:2048 nt
	s_nop 0
	global_load_dword v5, v193, s[44:45] nt
	global_load_dword v30, v[6:7], off offset:2048 nt
	global_load_dword v31, v194, s[44:45] nt
	s_nop 0
	global_load_dword v3, v[2:3], off offset:2048 nt
	v_mov_b32_e32 v6, 0
	s_mov_b64 s[44:45], 0
	v_mov_b32_e32 v2, v182
	v_mov_b32_e32 v7, 0
	v_mov_b32_e32 v10, 0
	v_mov_b32_e32 v11, 0
	v_mov_b32_e32 v12, 0
	v_mov_b32_e32 v13, 0
	v_mov_b32_e32 v14, 0
	v_mov_b32_e32 v15, 0
	v_mov_b32_e32 v16, 0
	v_mov_b32_e32 v17, 0
	v_mov_b32_e32 v18, 0
	s_waitcnt vmcnt(15)
	ds_write_b16 v164, v19
	s_waitcnt vmcnt(14)
	ds_write_b16 v165, v20
	s_waitcnt vmcnt(13)
	ds_write_b16 v166, v21
	s_waitcnt vmcnt(12)
	ds_write_b16 v167, v22
	s_waitcnt vmcnt(11)
	ds_write_b16 v168, v23
	s_waitcnt vmcnt(10)
	ds_write_b16 v169, v24
	s_waitcnt vmcnt(9)
	ds_write_b16 v170, v25
	s_waitcnt vmcnt(8)
	ds_write_b16 v171, v26
	s_waitcnt vmcnt(7)
	ds_write_b16 v172, v27
	s_waitcnt vmcnt(6)
	ds_write_b16 v173, v28
	s_waitcnt vmcnt(5)
	ds_write_b16 v174, v29
	s_waitcnt vmcnt(4)
	ds_write_b16 v175, v4
	s_waitcnt vmcnt(3)
	ds_write_b16 v176, v5
	s_waitcnt vmcnt(2)
	ds_write_b16 v177, v30
	s_waitcnt vmcnt(1)
	ds_write_b16 v178, v31
	s_waitcnt vmcnt(0)
	ds_write_b16 v179, v3
	v_mov_b32_e32 v19, 0
	v_mov_b32_e32 v20, 0
	v_mov_b32_e32 v21, 0
	s_waitcnt lgkmcnt(0)
	s_barrier
	s_branch .LBB0_1303
